# E row loop: two-deep prefetch via alternating load-target register sets, counted end-of-row wait, rotation copies removed
# speedup vs baseline: 1.0231x; 1.0026x over previous
; __device__ void phase_E_rows(const Params& p, int l, char* smem, int vb, int nvb, bool split, int nrows, int oz) {
;     ...
;     E2_LOAD(nx0, nxb0, ny0, rbeg)
;     if (rbeg + 1 < rend) E2_LOAD(nx1, nxb1, ny1, rbeg + 1)
;     for (int row = rbeg; row < rend; ++row) {
;         const bool isctx = row >= LAT;
;         const int mr = isctx ? 8 : row / T;
;         if (mr != cur_mr) {
;             cur_mr = mr;
; #pragma unroll
;             for (int k = 0; k < 4; ++k) {
;                 const int col = (k >> 1) * 512 + lane * 8 + (k & 1) * 4;
;                 if (l > 0) {
;                     const float4 g = *(const float4*)(mod + ((l - 1) * 9 + mr) * 3072 + 2048 + col);
;                     const float4 pg = *(const float4*)(p.in[I_POSTG] + (l - 1) * DM + col);
;                     gp[k] = make_float4(g.x * pg.x, g.y * pg.y, g.z * pg.z, g.w * pg.w);
;                 }
;                 if (l < 4) {
;                     const float4 pre = *(const float4*)(p.in[I_PREG] + l * DM + col);
;                     const float4 sc = *(const float4*)(mod + (l * 9 + mr) * 3072 + 1024 + col);
;                     sh[k] = *(const float4*)(mod + (l * 9 + mr) * 3072 + col);
;                     pa[k] = make_float4(pre.x * (1.f + sc.x), pre.y * (1.f + sc.y), pre.z * (1.f + sc.z), pre.w * (1.f + sc.w));
;                 }
;             }
.LBB0_913:
	s_waitcnt vmcnt(0)
	v_mov_b64_e32 v[86:87], v[82:83]
	s_add_u32 s64, s78, s20
	v_mov_b64_e32 v[90:91], v[74:75]
	v_mov_b64_e32 v[94:95], v[78:79]
	v_mov_b64_e32 v[98:99], v[70:71]
	v_mov_b64_e32 v[84:85], v[80:81]
	s_addc_u32 s65, s79, s21
	s_mov_b32 s28, -1
	v_mov_b64_e32 v[88:89], v[72:73]
	v_mov_b64_e32 v[92:93], v[76:77]
	v_mov_b64_e32 v[96:97], v[68:69]
	v_mov_b64_e32 v[150:151], v[64:65]
	v_mov_b64_e32 v[152:153], v[66:67]
	v_mov_b64_e32 v[154:155], v[60:61]
	v_mov_b64_e32 v[156:157], v[62:63]
	v_mov_b64_e32 v[158:159], v[56:57]
	v_mov_b64_e32 v[160:161], v[58:59]
	v_mov_b64_e32 v[162:163], v[52:53]
	v_mov_b64_e32 v[164:165], v[54:55]
	v_mov_b32_e32 v234, 0
.LBB0_914:
	s_ashr_i32 s20, s56, 31
	s_lshr_b32 s20, s20, 21
	s_add_i32 s20, s56, s20
	s_ashr_i32 s29, s20, 11
	s_cmpk_gt_i32 s56, 0x3fff
	s_cselect_b64 s[20:21], -1, 0
	s_and_b64 s[46:47], s[20:21], exec
	s_cselect_b32 s66, 8, s29
	s_cmp_eq_u32 s66, s28
	s_cbranch_scc1 .LBB0_931
	s_add_i32 s28, s66, s48
	s_mulk_i32 s28, 0xc00
	s_ashr_i32 s29, s28, 31
	s_lshl_b64 s[28:29], s[28:29], 2
	s_add_u32 s28, s60, s28
	s_addc_u32 s29, s61, s29
	s_add_u32 s84, s28, 0x2000
	s_addc_u32 s85, s29, 0
	s_add_i32 s28, s66, s49
	s_mulk_i32 s28, 0xc00
	s_ashr_i32 s29, s28, 31
	s_lshl_b64 s[28:29], s[28:29], 2
	s_add_u32 s28, s60, s28
	s_addc_u32 s29, s61, s29
	s_add_u32 s82, s28, 0x1000
	v_cndmask_b32_e64 v245, 0, 1, s[50:51]
	s_addc_u32 s83, s29, 0
	v_cmp_ne_u32_e64 s[46:47], 1, v245
	v_lshlrev_b32_e32 v242, 2, v106
	v_lshlrev_b32_e32 v243, 2, v108
	v_lshlrev_b32_e32 v244, 2, v110
	s_and_b64 vcc, exec, s[44:45]
	s_cbranch_vccnz .Le_mod_noA
	global_load_dwordx4 v[118:121], v2, s[84:85]
	global_load_dwordx4 v[202:205], v[112:113], off
	global_load_dwordx4 v[122:125], v242, s[84:85]
	global_load_dwordx4 v[206:209], v[112:113], off offset:16
	global_load_dwordx4 v[126:129], v243, s[84:85]
	global_load_dwordx4 v[210:213], v[112:113], off offset:2048
	global_load_dwordx4 v[134:137], v244, s[84:85]
	global_load_dwordx4 v[214:217], v[112:113], off offset:2064
.Le_mod_noA:
	s_andn2_b64 vcc, exec, s[50:51]
	s_cbranch_vccnz .Le_mod_noB
	global_load_dwordx4 v[218:221], v2, s[82:83]
	global_load_dwordx4 v[222:225], v[114:115], off
	global_load_dwordx4 v[4:7], v2, s[28:29]
	global_load_dwordx4 v[226:229], v242, s[82:83]
	global_load_dwordx4 v[230:233], v[114:115], off offset:16
	global_load_dwordx4 v[8:11], v2, s[28:29] offset:16
	global_load_dwordx4 v[184:187], v243, s[82:83]
	global_load_dwordx4 v[188:191], v[114:115], off offset:2048
	global_load_dwordx4 v[12:15], v2, s[28:29] offset:2048
	global_load_dwordx4 v[192:195], v244, s[82:83]
	global_load_dwordx4 v[238:241], v[114:115], off offset:2064
	global_load_dwordx4 v[16:19], v2, s[28:29] offset:2064

; __device__ void phase_E_rows(const Params& p, int l, char* smem, int vb, int nvb, bool split, int nrows, int oz) {
;     ...
;                 if (l < 4) {
;                     const float4 pre = *(const float4*)(p.in[I_PREG] + l * DM + col);
;                     const float4 sc = *(const float4*)(mod + (l * 9 + mr) * 3072 + 1024 + col);
;                     sh[k] = *(const float4*)(mod + (l * 9 + mr) * 3072 + col);
;                     pa[k] = make_float4(pre.x * (1.f + sc.x), pre.y * (1.f + sc.y), pre.z * (1.f + sc.z), pre.w * (1.f + sc.w));
;                 }
.Le_mod_cA:
	s_andn2_b64 vcc, exec, s[50:51]
	s_cbranch_vccnz .LBB0_932
	v_pk_add_f32 v[218:219], v[218:219], 1.0 op_sel_hi:[1,0]
	v_pk_add_f32 v[220:221], v[220:221], 1.0 op_sel_hi:[1,0]
	v_pk_mul_f32 v[132:133], v[222:223], v[218:219]
	v_pk_mul_f32 v[130:131], v[224:225], v[220:221]
	v_pk_add_f32 v[226:227], v[226:227], 1.0 op_sel_hi:[1,0]
	v_pk_add_f32 v[228:229], v[228:229], 1.0 op_sel_hi:[1,0]
	v_pk_mul_f32 v[140:141], v[230:231], v[226:227]
	v_pk_mul_f32 v[138:139], v[232:233], v[228:229]
	v_pk_add_f32 v[184:185], v[184:185], 1.0 op_sel_hi:[1,0]
	v_pk_add_f32 v[186:187], v[186:187], 1.0 op_sel_hi:[1,0]
	v_pk_mul_f32 v[144:145], v[188:189], v[184:185]
	v_pk_mul_f32 v[142:143], v[190:191], v[186:187]
	v_pk_add_f32 v[192:193], v[192:193], 1.0 op_sel_hi:[1,0]
	v_pk_add_f32 v[194:195], v[194:195], 1.0 op_sel_hi:[1,0]
	v_pk_mul_f32 v[146:147], v[238:239], v[192:193]
	v_pk_mul_f32 v[148:149], v[240:241], v[194:195]
	s_branch .LBB0_932

; __device__ void phase_E_rows(const Params& p, int l, char* smem, int vb, int nvb, bool split, int nrows, int oz) {
;     ...
;         for (int k = 0; k < 4; ++k) nx0[k] = nx1[k];
; #pragma unroll
;         for (int k2 = 0; k2 < 2; ++k2) { yq[k2] = ny0[k2]; nxb0[k2] = nxb1[k2]; ny0[k2] = ny1[k2]; }
;         if (row + 2 < rend) E2_LOAD(nx1, nxb1, ny1, row + 2)
.LBB0_932:
	s_add_i32 s28, s56, 2
	s_cmp_ge_i32 s28, s27
	s_cbranch_scc1 .LBB0_957
	s_cmpk_lt_i32 s56, 0x3ffe
	s_mov_b64 s[80:81], -1
	s_cselect_b64 s[82:83], -1, 0
	s_and_b64 vcc, exec, s[0:1]
	s_cbranch_vccz .LBB0_939
	s_and_b64 vcc, exec, s[82:83]
	s_cbranch_vccz .LBB0_936
	v_readlane_b32 s4, v253, 18
	s_ashr_i32 s29, s28, 31
	v_readlane_b32 s18, v253, 32
	v_readlane_b32 s19, v253, 33
	s_mov_b64 s[80:81], 0
	v_readlane_b32 s5, v253, 19
	v_readlane_b32 s6, v253, 20
	v_readlane_b32 s7, v253, 21
	v_readlane_b32 s8, v253, 22
	v_readlane_b32 s9, v253, 23
	v_readlane_b32 s10, v253, 24
	v_readlane_b32 s11, v253, 25
	v_readlane_b32 s12, v253, 26
	v_readlane_b32 s13, v253, 27
	v_readlane_b32 s14, v253, 28
	v_readlane_b32 s15, v253, 29
	v_readlane_b32 s16, v253, 30
	v_readlane_b32 s17, v253, 31
	s_mov_b64 s[46:47], s[18:19]
	s_mov_b64 s[18:19], s[88:89]
	s_mov_b64 s[84:85], s[28:29]

.LBB0_944:
	s_lshl_b64 s[68:69], s[84:85], 12
	s_add_u32 s46, s46, s68
	s_addc_u32 s47, s47, s69
	v_lshl_add_u64 v[184:185], s[46:47], 0, v[2:3]
	v_lshl_add_u64 v[186:187], v[184:185], 0, v[116:117]
	s_ashr_i32 s29, s28, 31
	s_lshl_b64 s[28:29], s[28:29], 11
	v_lshl_add_u64 v[188:189], v[104:105], 0, s[28:29]
	s_mov_b32 s80, s86
	v_readfirstlane_b32 s96, v234
	s_nop 0
	s_cmp_eq_u32 s96, 0
	s_cbranch_scc0 .Le2_ldB
	s_and_b64 vcc, exec, s[40:41]
	s_cbranch_vccnz .Le2_nf_A
	global_load_dwordx4 v[52:55], v[184:185], off nt
	global_load_dwordx4 v[56:59], v[184:185], off offset:16 nt
	global_load_dwordx4 v[60:63], v[184:185], off offset:2048 nt
	global_load_dwordx4 v[64:67], v[184:185], off offset:2064 nt
.Le2_nf_A:
	s_and_b64 vcc, exec, s[42:43]
	s_cbranch_vccnz .Le2_nx_A
	global_load_dwordx4 v[68:71], v[186:187], off offset:2048 nt
	global_load_dwordx4 v[76:79], v[186:187], off offset:3072 nt
.Le2_nx_A:
	s_and_b64 vcc, exec, s[44:45]
	s_cbranch_vccnz .LBB0_957
	global_load_dwordx4 v[72:75], v[188:189], off nt
	global_load_dwordx4 v[80:83], v[188:189], off offset:1024 nt
	s_branch .LBB0_957
.Le2_ldB:
	s_and_b64 vcc, exec, s[40:41]
	s_cbranch_vccnz .Le2_nf_B
	global_load_dwordx4 v[162:165], v[184:185], off nt
	global_load_dwordx4 v[158:161], v[184:185], off offset:16 nt
	global_load_dwordx4 v[154:157], v[184:185], off offset:2048 nt
	global_load_dwordx4 v[150:153], v[184:185], off offset:2064 nt
.Le2_nf_B:
	s_and_b64 vcc, exec, s[42:43]
	s_cbranch_vccnz .Le2_nx_B
	global_load_dwordx4 v[96:99], v[186:187], off offset:2048 nt
	global_load_dwordx4 v[92:95], v[186:187], off offset:3072 nt
.Le2_nx_B:
	s_and_b64 vcc, exec, s[44:45]
	s_cbranch_vccnz .LBB0_957
	global_load_dwordx4 v[88:91], v[188:189], off nt
	global_load_dwordx4 v[84:87], v[188:189], off offset:1024 nt

; __device__ __forceinline__ float h_lo(unsigned u) { return (float)__builtin_bit_cast(f16v2, u)[0]; }
; __device__ __forceinline__ float h_hi(unsigned u) { return (float)__builtin_bit_cast(f16v2, u)[1]; }
; __device__ void phase_E_rows(const Params& p, int l, char* smem, int vb, int nvb, bool split, int nrows, int oz) {
;     ...
;     for (int row = rbeg; row < rend; ++row) {
;         const bool isctx = row >= LAT;
;         const int mr = isctx ? 8 : row / T;
;         if (mr != cur_mr) {
;             cur_mr = mr;
; #pragma unroll
;             for (int k = 0; k < 4; ++k) {
;                 const int col = (k >> 1) * 512 + lane * 8 + (k & 1) * 4;
;                 if (l > 0) {
;                     const float4 g = *(const float4*)(mod + ((l - 1) * 9 + mr) * 3072 + 2048 + col);
;                     const float4 pg = *(const float4*)(p.in[I_POSTG] + (l - 1) * DM + col);
;                     gp[k] = make_float4(g.x * pg.x, g.y * pg.y, g.z * pg.z, g.w * pg.w);
;                 }
;                 if (l < 4) {
;                     const float4 pre = *(const float4*)(p.in[I_PREG] + l * DM + col);
;                     const float4 sc = *(const float4*)(mod + (l * 9 + mr) * 3072 + 1024 + col);
;                     sh[k] = *(const float4*)(mod + (l * 9 + mr) * 3072 + col);
;                     pa[k] = make_float4(pre.x * (1.f + sc.x), pre.y * (1.f + sc.y), pre.z * (1.f + sc.z), pre.w * (1.f + sc.w));
;                 }
;             }
;         }
;         float* xcur = isctx ? XC + (size_t)(row - LAT) * DM : p.out + (size_t)row * DM;
;         float4 xv[4];
;         u32x4 yq[2];
; #pragma unroll
;         for (int k = 0; k < 4; ++k) {
;             const u32x4 w = nxb0[k >> 1];
;             const int h2 = 2 * (k & 1);
;             xv[k] = (l <= 1) ? nx0[k] : make_float4(h_lo(w[h2]), h_hi(w[h2]), h_lo(w[h2 + 1]), h_hi(w[h2 + 1]));
;         }
; #pragma unroll
;         for (int k = 0; k < 4; ++k) nx0[k] = nx1[k];
; #pragma unroll
;         for (int k2 = 0; k2 < 2; ++k2) { yq[k2] = ny0[k2]; nxb0[k2] = nxb1[k2]; ny0[k2] = ny1[k2]; }
.LBB0_964:
	s_add_u32 s56, s56, 1
	s_addc_u32 s57, s57, 0
	s_add_u32 s64, s64, 0x800
	s_addc_u32 s65, s65, 0
	s_cmp_lt_i32 s56, s27
	s_cbranch_scc0 .LBB0_841
	s_add_i32 s96, s56, 1
	s_cmp_lt_i32 s96, s27
	s_cselect_b32 s96, 1, 0
	s_and_b64 vcc, exec, s[44:45]
	s_cbranch_vccnz .Le2_w_l0
	s_and_b64 vcc, exec, s[40:41]
	s_cbranch_vccnz .Le2_w_l2
	s_cmp_eq_u32 s96, 1
	s_cbranch_scc1 .Le2_w14
	s_waitcnt vmcnt(8)
	s_branch .Le2_wd
.Le2_w14:
	s_waitcnt vmcnt(14)
	s_branch .Le2_wd
.Le2_w_l0:
	s_cmp_eq_u32 s96, 1
	s_cbranch_scc1 .Le2_w8
	s_waitcnt vmcnt(4)
	s_branch .Le2_wd
.Le2_w8:
	s_waitcnt vmcnt(8)
	s_branch .Le2_wd
.Le2_w_l2:
	s_cmp_eq_u32 s96, 1
	s_cbranch_scc1 .Le2_w12
	s_waitcnt vmcnt(8)
	s_branch .Le2_wd
.Le2_w12:
	s_waitcnt vmcnt(12)
.Le2_wd:
	v_readfirstlane_b32 s96, v234
	v_xor_b32_e32 v234, 1, v234
	s_cmp_eq_u32 s96, 0
	s_cbranch_scc0 .Le2_cpA
	v_mov_b64_e32 v[24:25], v[96:97]
	v_mov_b64_e32 v[26:27], v[98:99]
	v_mov_b64_e32 v[48:49], v[88:89]
	v_mov_b64_e32 v[50:51], v[90:91]
	v_mov_b64_e32 v[20:21], v[92:93]
	v_mov_b64_e32 v[22:23], v[94:95]
	v_mov_b64_e32 v[44:45], v[84:85]
	v_mov_b64_e32 v[46:47], v[86:87]
	v_mov_b64_e32 v[40:41], v[162:163]
	v_mov_b64_e32 v[42:43], v[164:165]
	v_mov_b64_e32 v[36:37], v[158:159]
	v_mov_b64_e32 v[38:39], v[160:161]
	v_mov_b64_e32 v[32:33], v[154:155]
	v_mov_b64_e32 v[34:35], v[156:157]
	v_mov_b64_e32 v[28:29], v[150:151]
	v_mov_b64_e32 v[30:31], v[152:153]
	s_branch .Le2_cpd
.Le2_cpA:
	v_mov_b64_e32 v[24:25], v[68:69]
	v_mov_b64_e32 v[26:27], v[70:71]
	v_mov_b64_e32 v[48:49], v[72:73]
	v_mov_b64_e32 v[50:51], v[74:75]
	v_mov_b64_e32 v[20:21], v[76:77]
	v_mov_b64_e32 v[22:23], v[78:79]
	v_mov_b64_e32 v[44:45], v[80:81]
	v_mov_b64_e32 v[46:47], v[82:83]
	v_mov_b64_e32 v[40:41], v[52:53]
	v_mov_b64_e32 v[42:43], v[54:55]
	v_mov_b64_e32 v[36:37], v[56:57]
	v_mov_b64_e32 v[38:39], v[58:59]
	v_mov_b64_e32 v[32:33], v[60:61]
	v_mov_b64_e32 v[34:35], v[62:63]
	v_mov_b64_e32 v[28:29], v[64:65]
	v_mov_b64_e32 v[30:31], v[66:67]
.Le2_cpd:
	s_mov_b32 s28, s66
	s_branch .LBB0_914
